# speedup vs baseline: 1.0260x; 1.0077x over previous
.LBB0_8:
	s_load_dwordx4 s[8:11], s[0:1], 0x0
	s_load_dwordx2 s[12:13], s[0:1], 0x10
	v_lshrrev_b32_e32 v6, 6, v0
	v_lshl_or_b32 v1, s2, 2, v6
	s_movk_i32 s0, 0xc2
	v_and_b32_e32 v28, 63, v0
	v_mul_lo_u32 v2, v1, s0
	v_mov_b32_e32 v3, 0
	s_waitcnt lgkmcnt(0)
	v_lshl_add_u64 v[4:5], v[2:3], 2, s[10:11]
	v_lshlrev_b32_e32 v2, 2, v28
	v_lshl_add_u64 v[4:5], v[4:5], 0, v[2:3]
	global_load_dword v124, v[4:5], off nt
	global_load_dword v125, v[4:5], off offset:256 nt
	global_load_dword v126, v[4:5], off offset:512 nt
	v_lshlrev_b32_e32 v30, 10, v6
	v_or_b32_e32 v128, v30, v2
	v_cmp_gt_u32_e64 s[46:47], 2, v28
	v_cmp_gt_u32_e32 vcc, 2, v28
	s_and_saveexec_b64 s[0:1], vcc
	s_cbranch_execz .Lsim_notail
	global_load_dword v127, v[4:5], off offset:768 nt
.Lsim_notail:
	s_or_b64 exec, exec, s[0:1]
	v_lshl_or_b32 v58, v1, 8, v28
	v_mov_b32_e32 v59, 0
	v_lshl_add_u64 v[58:59], v[58:59], 2, s[8:9]
	global_load_dword v54, v[58:59], off nt
	global_load_dword v53, v[58:59], off offset:256 nt
	global_load_dword v52, v[58:59], off offset:512 nt
	global_load_dword v55, v[58:59], off offset:768 nt
	v_lshlrev_b32_e32 v22, 2, v0
	v_and_b32_e32 v6, 15, v0
	v_and_b32_e32 v2, 0xc0, v22
	v_or_b32_e32 v18, v2, v6
	v_lshrrev_b32_e32 v4, 1, v18
	v_bcnt_u32_b32 v19, v6, 0
	v_bitop3_b32 v2, v4, v2, v6 bitop3:0xe0
	v_bcnt_u32_b32 v2, v2, v19
	v_and_b32_e32 v2, 1, v2
	v_cmp_eq_u32_e32 vcc, 0, v2
	v_or_b32_e32 v2, 16, v18
	v_lshrrev_b32_e32 v2, 1, v2
	v_bitop3_b32 v2, v2, v18, 16 bitop3:0xe0
	v_bcnt_u32_b32 v2, v2, v19
	v_and_b32_e32 v2, 1, v2
	v_cmp_eq_u32_e64 s[0:1], 0, v2
	v_bitop3_b32 v2, v4, v18, 32 bitop3:0xe0
	v_bcnt_u32_b32 v2, v2, v19
	v_and_b32_e32 v2, 1, v2
	v_cmp_eq_u32_e64 s[2:3], 0, v2
	v_or_b32_e32 v2, 48, v18
	v_lshrrev_b32_e32 v2, 1, v2
	v_bitop3_b32 v2, v2, v18, 48 bitop3:0xe0
	v_bcnt_u32_b32 v2, v2, v19
	v_and_b32_e32 v2, 1, v2
	v_mov_b32_e32 v5, 0xbd800000
	v_mov_b32_e32 v10, 0x3d800000
	v_cmp_eq_u32_e64 s[4:5], 0, v2
	v_mov_b32_e32 v20, 0xbd3504f3
	v_mov_b32_e32 v21, 0x3d3504f3
	v_or_b32_e32 v2, 0x100, v18
	v_cndmask_b32_e64 v8, v5, v10, s[0:1]
	v_cndmask_b32_e64 v12, v20, v21, s[0:1]
	s_movk_i32 s0, 0x100
	v_lshrrev_b32_e32 v2, 1, v2
	v_bitop3_b32 v2, v2, v18, s0 bitop3:0xe0
	v_bcnt_u32_b32 v2, v2, v19
	v_and_b32_e32 v2, 1, v2
	v_cndmask_b32_e32 v7, v5, v10, vcc
	v_cndmask_b32_e32 v11, v20, v21, vcc
	v_cmp_eq_u32_e32 vcc, 0, v2
	v_or_b32_e32 v2, 0x110, v18
	s_movk_i32 s0, 0x110
	v_lshrrev_b32_e32 v2, 1, v2
	v_bitop3_b32 v2, v2, v18, s0 bitop3:0xe0
	v_bcnt_u32_b32 v2, v2, v19
	v_and_b32_e32 v2, 1, v2
	v_cndmask_b32_e32 v15, v20, v21, vcc
	v_cmp_eq_u32_e32 vcc, 0, v2
	v_or_b32_e32 v2, 0x120, v18
	s_movk_i32 s0, 0x120
	v_lshrrev_b32_e32 v2, 1, v2
	v_bitop3_b32 v2, v2, v18, s0 bitop3:0xe0
	v_bcnt_u32_b32 v17, v2, v19
	v_lshl_or_b32 v2, v1, 8, v28
	v_cndmask_b32_e64 v9, v5, v10, s[2:3]
	v_cndmask_b32_e64 v10, v5, v10, s[4:5]
	v_and_b32_e32 v2, 1, v17
	v_cndmask_b32_e32 v16, v20, v21, vcc
	v_cmp_eq_u32_e32 vcc, 0, v2
	v_or_b32_e32 v2, 0x130, v18
	s_movk_i32 s0, 0x130
	v_lshrrev_b32_e32 v2, 1, v2
	v_bitop3_b32 v2, v2, v18, s0 bitop3:0xe0
	v_bcnt_u32_b32 v2, v2, v19
	v_and_b32_e32 v2, 1, v2
	v_cndmask_b32_e32 v17, v20, v21, vcc
	v_cmp_eq_u32_e32 vcc, 0, v2
	v_cndmask_b32_e64 v13, v20, v21, s[2:3]
	v_cndmask_b32_e64 v14, v20, v21, s[4:5]
	v_cndmask_b32_e32 v18, v20, v21, vcc
	v_and_b32_e32 v20, 3, v0
	s_movk_i32 s6, 0xc0
	s_movk_i32 s2, 0x80
	v_bfrev_b32_e32 v2, 0.5
	v_bcnt_u32_b32 v20, v20, 0
	v_bitop3_b32 v19, v22, s2, v2 bitop3:0x6c
	v_and_b32_e32 v5, 12, v0
	v_lshlrev_b32_e32 v40, 2, v20
	v_bitop3_b32 v20, v22, s6, v2 bitop3:0x6c
	v_lshrrev_b32_e32 v2, 3, v0
	v_and_b32_e32 v23, 6, v0
	v_and_b32_e32 v24, 2, v0
	v_cmp_gt_u32_e64 s[0:1], 32, v28
	v_and_b32_e32 v4, 48, v0
	v_bcnt_u32_b32 v5, v5, 0
	v_and_b32_e32 v21, 4, v2
	v_and_b32_e32 v2, 24, v0
	v_bcnt_u32_b32 v23, v23, 0
	v_cmp_eq_u32_e32 vcc, 0, v24
	v_and_b32_e32 v25, 4, v0
	v_lshrrev_b32_e32 v28, 4, v28
	v_bcnt_u32_b32 v4, v4, 0
	v_and_b32_e32 v5, 1, v5
	v_bcnt_u32_b32 v2, v2, 0
	v_lshlrev_b32_e32 v37, 2, v23
	v_and_b32_e32 v23, 1, v0
	v_cndmask_b32_e64 v24, -1.0, 1.0, vcc
	v_cmp_eq_u32_e32 vcc, 0, v25
	v_and_b32_e32 v26, 8, v0
	v_bfe_u32 v27, v0, 1, 3
	v_mul_u32_u24_e32 v28, 33, v28
	v_lshlrev_b32_e32 v31, 3, v0
	v_lshlrev_b32_e32 v4, 2, v4
	v_lshlrev_b32_e32 v5, 2, v5
	v_lshlrev_b32_e32 v2, 2, v2
	v_cmp_eq_u32_e64 s[2:3], 0, v23
	v_cndmask_b32_e64 v25, -1.0, 1.0, vcc
	v_cmp_eq_u32_e32 vcc, 0, v26
	v_mul_u32_u24_e32 v27, 3, v27
	v_lshl_add_u32 v29, v28, 2, v30
	v_and_b32_e32 v31, 0x80, v31
	v_and_b32_e32 v22, 4, v22
	v_cndmask_b32_e64 v23, -1.0, 1.0, s[2:3]
	v_cndmask_b32_e64 v26, -1.0, 1.0, vcc
	v_cmp_gt_u32_e64 s[4:5], 8, v6
	v_lshl_add_u32 v28, v27, 2, v29
	v_cmp_gt_u32_e64 s[6:7], 9, v6
	v_lshl_add_u32 v29, v6, 2, v29
	v_add_u32_e32 v30, v30, v31
	v_or_b32_e32 v31, 8, v4
	v_or_b32_e32 v32, 16, v5
	v_or_b32_e32 v33, 24, v40
	v_or_b32_e32 v34, 40, v2
	v_and_or_b32 v35, v37, 4, 48
	v_and_or_b32 v36, v2, 4, 16
	v_or_b32_e32 v37, 24, v37
	v_or_b32_e32 v38, 40, v4
	v_or_b32_e32 v39, 48, v5
	v_or_b32_e32 v40, 56, v40
	s_mov_b64 s[8:9], -1
	s_mov_b32 s16, 0x219392ef
	s_mov_b32 s17, 0xf800000
	v_mov_b32_e32 v41, 0x260
	v_mov_b32_e32 v42, 0x3c23d70a
	v_mov_b32_e32 v43, 0x219392ef
	v_mov_b32_e32 v44, 0xa19392ef
	v_mov_b32_e32 v57, 0
	v_mov_b32_e32 v56, 0
	v_mov_b32_e32 v58, 0
	s_waitcnt vmcnt(5)
	ds_write2st64_b32 v128, v124, v125 offset1:1
	ds_write_b32 v128, v126 offset:512
	s_waitcnt vmcnt(4)
	s_and_saveexec_b64 s[48:49], s[46:47]
	s_cbranch_execz .Lsim_staged
	ds_write_b32 v128, v127 offset:768
.Lsim_staged:
	s_or_b64 exec, exec, s[48:49]
	s_branch .LBB0_12

	.amdhsa_kernel _Z15sim_prep_kernelPKfS0_PDF16_S0_S1_
		.amdhsa_group_segment_fixed_size 43008
		.amdhsa_private_segment_fixed_size 0
		.amdhsa_kernarg_size 40
		.amdhsa_user_sgpr_count 2
		.amdhsa_user_sgpr_dispatch_ptr 0
		.amdhsa_user_sgpr_queue_ptr 0
		.amdhsa_user_sgpr_kernarg_segment_ptr 1
		.amdhsa_user_sgpr_dispatch_id 0
		.amdhsa_user_sgpr_kernarg_preload_length 0
		.amdhsa_user_sgpr_kernarg_preload_offset 0
		.amdhsa_user_sgpr_private_segment_size 0
		.amdhsa_uses_dynamic_stack 0
		.amdhsa_enable_private_segment 0
		.amdhsa_system_sgpr_workgroup_id_x 1
		.amdhsa_system_sgpr_workgroup_id_y 0
		.amdhsa_system_sgpr_workgroup_id_z 0
		.amdhsa_system_sgpr_workgroup_info 0
		.amdhsa_system_vgpr_workitem_id 0
		.amdhsa_next_free_vgpr 136
		.amdhsa_next_free_sgpr 96
		.amdhsa_accum_offset 132
		.amdhsa_reserve_vcc 1
		.amdhsa_float_round_mode_32 0
		.amdhsa_float_round_mode_16_64 0
		.amdhsa_float_denorm_mode_32 3
		.amdhsa_float_denorm_mode_16_64 3
		.amdhsa_dx10_clamp 1
		.amdhsa_ieee_mode 1
		.amdhsa_fp16_overflow 0
		.amdhsa_tg_split 0
		.amdhsa_exception_fp_ieee_invalid_op 0
		.amdhsa_exception_fp_denorm_src 0
		.amdhsa_exception_fp_ieee_div_zero 0
		.amdhsa_exception_fp_ieee_overflow 0
		.amdhsa_exception_fp_ieee_underflow 0
		.amdhsa_exception_fp_ieee_inexact 0
		.amdhsa_exception_int_div_zero 0
	.end_amdhsa_kernel

amdhsa.kernels:
  - .agpr_count:     0
    .args:
      - .actual_access:  read_only
        .address_space:  global
        .offset:         0
        .size:           8
        .value_kind:     global_buffer
      - .actual_access:  read_only
        .address_space:  global
        .offset:         8
        .size:           8
        .value_kind:     global_buffer
      - .actual_access:  write_only
        .address_space:  global
        .offset:         16
        .size:           8
        .value_kind:     global_buffer
      - .actual_access:  read_only
        .address_space:  global
        .offset:         24
        .size:           8
        .value_kind:     global_buffer
      - .actual_access:  write_only
        .address_space:  global
        .offset:         32
        .size:           8
        .value_kind:     global_buffer
    .group_segment_fixed_size: 43008
    .kernarg_segment_align: 8
    .kernarg_segment_size: 40
    .language:       OpenCL C
    .language_version:
      - 2
      - 0
    .max_flat_workgroup_size: 256
    .name:           _Z15sim_prep_kernelPKfS0_PDF16_S0_S1_
    .private_segment_fixed_size: 0
    .sgpr_count:     43
    .sgpr_spill_count: 0
    .symbol:         _Z15sim_prep_kernelPKfS0_PDF16_S0_S1_.kd
    .uniform_work_group_size: 1
    .uses_dynamic_stack: false
    .vgpr_count:     129
    .vgpr_spill_count: 0
    .wavefront_size: 64
  - .agpr_count:     0
    .args:
      - .address_space:  global
        .offset:         0
        .size:           8
        .value_kind:     global_buffer
      - .address_space:  global
        .offset:         8
        .size:           8
        .value_kind:     global_buffer
      - .actual_access:  write_only
        .address_space:  global
        .offset:         16
        .size:           8
        .value_kind:     global_buffer
    .group_segment_fixed_size: 114688
    .kernarg_segment_align: 8
    .kernarg_segment_size: 24
    .language:       OpenCL C
    .language_version:
      - 2
      - 0
    .max_flat_workgroup_size: 512
    .name:           _Z9feat_gemmPKDF16_S0_PDF16_
    .private_segment_fixed_size: 0
    .sgpr_count:     53
    .sgpr_spill_count: 0
    .symbol:         _Z9feat_gemmPKDF16_S0_PDF16_.kd
    .uniform_work_group_size: 1
    .uses_dynamic_stack: false
    .vgpr_count:     192
    .vgpr_spill_count: 0
    .wavefront_size: 64
  - .agpr_count:     0
    .args:
      - .actual_access:  read_only
        .address_space:  global
        .offset:         0
        .size:           8
        .value_kind:     global_buffer
      - .actual_access:  write_only
        .address_space:  global
        .offset:         8
        .size:           8
        .value_kind:     global_buffer
    .group_segment_fixed_size: 0
    .kernarg_segment_align: 8
    .kernarg_segment_size: 16
    .language:       OpenCL C
    .language_version:
      - 2
      - 0
    .max_flat_workgroup_size: 256
    .name:           _Z13reduce_kernelPKDF16_Pf
    .private_segment_fixed_size: 0
    .sgpr_count:     25
    .sgpr_spill_count: 0
    .symbol:         _Z13reduce_kernelPKDF16_Pf.kd
    .uniform_work_group_size: 1
    .uses_dynamic_stack: false
    .vgpr_count:     78
    .vgpr_spill_count: 0
    .wavefront_size: 64
